# v045 with the fused conversion's fp8 result stores write-back instead of non-temporal
# baseline (speedup 1.0000x reference)
.Lfz_s_skip:
	s_nop 0
	v_mov_b32_e32 v56, v0
	s_and_b32 s1, s82, 0x400
	s_lshl_b32 s0, s85, 8
	v_and_b32_e32 v54, 15, v56
	s_add_i32 s1, s76, s1
	s_add_i32 s0, s0, s7
	v_lshl_add_u32 v132, v54, 2, s1
	v_or_b32_e32 v130, s0, v54
	ds_read2_b32 v[54:55], v132 offset1:16
	s_lshl_b32 s0, s84, 7
	s_and_b32 s0, s0, 0x780
	v_lshrrev_b32_e32 v56, 1, v56
	v_and_or_b32 v56, v56, 24, s0
	s_waitcnt lgkmcnt(0)
	v_mul_f32_e32 v54, 0x3b800000, v54
	v_pk_mul_f32 v[62:63], v[122:123], v[54:55] op_sel_hi:[1,0]
	v_pk_mul_f32 v[86:87], v[118:119], v[54:55] op_sel_hi:[1,0]
	v_mul_f32_e32 v92, 0xbfb8aa3b, v62
	v_exp_f32_e32 v118, v92
	v_pk_mul_f32 v[92:93], v[116:117], v[54:55] op_sel_hi:[1,0]
	v_mul_f32_e32 v116, 0xbfb8aa3b, v63
	v_exp_f32_e32 v116, v116
	v_or_b32_e32 v206, s6, v56
	v_pk_mul_f32 v[56:57], v[124:125], v[54:55] op_sel_hi:[1,0]
	v_pk_mul_f32 v[64:65], v[120:121], v[54:55] op_sel_hi:[1,0]
	v_pk_mul_f32 v[88:89], v[128:129], v[54:55] op_sel_hi:[1,0]
	v_pk_mul_f32 v[90:91], v[126:127], v[54:55] op_sel_hi:[1,0]
	v_add_f32_e32 v117, 1.0, v118
	v_pk_mul_f32 v[114:115], v[114:115], v[54:55] op_sel_hi:[1,0]
	v_add_f32_e32 v54, 1.0, v116
	v_rcp_f32_e32 v117, v117
	v_rcp_f32_e32 v54, v54
	v_ashrrev_i32_e32 v131, 31, v130
	s_mov_b32 s0, 0x40000
	v_mul_f32_e32 v62, v62, v117
	v_mul_f32_e32 v54, v63, v54
	v_mul_f32_e32 v63, 0xbfb8aa3b, v56
	v_mul_f32_e32 v62, v90, v62
	v_exp_f32_e32 v63, v63
	v_mul_f32_e32 v90, 0xbfb8aa3b, v57
	v_exp_f32_e32 v90, v90
	v_mul_f32_e32 v62, 0x41000000, v62
	v_add_f32_e32 v63, 1.0, v63
	v_rcp_f32_e32 v63, v63
	v_add_f32_e32 v90, 1.0, v90
	v_rcp_f32_e32 v90, v90
	v_mul_f32_e32 v54, v91, v54
	v_mul_f32_e32 v56, v56, v63
	v_mul_f32_e32 v54, 0x41000000, v54
	v_mul_f32_e32 v56, v88, v56
	v_mul_f32_e32 v57, v57, v90
	v_min_f32_e64 v63, |v62|, s33
	v_mul_f32_e32 v88, 0xbfb8aa3b, v86
	v_mul_f32_e32 v56, 0x41000000, v56
	v_mul_f32_e32 v57, v89, v57
	v_bfi_b32 v62, s2, v63, v62
	v_min_f32_e64 v63, |v54|, s33
	v_exp_f32_e32 v88, v88
	v_mul_f32_e32 v57, 0x41000000, v57
	v_bfi_b32 v54, s2, v63, v54
	v_min_f32_e64 v63, |v56|, s33
	v_bfi_b32 v63, s2, v63, v56
	v_min_f32_e64 v56, |v57|, s33
	v_bfi_b32 v57, s2, v56, v57
	v_mov_b32_e32 v56, v207
	v_cvt_pk_fp8_f32 v56, v62, v54
	v_add_f32_e32 v62, 1.0, v88
	v_rcp_f32_e32 v62, v62
	v_mul_f32_e32 v54, 0xbfb8aa3b, v87
	v_exp_f32_e32 v54, v54
	v_cvt_pk_fp8_f32 v56, v63, v57 op_sel:[0,0,1]
	v_mul_f32_e32 v57, v86, v62
	v_mul_f32_e32 v62, 0xbfb8aa3b, v64
	v_exp_f32_e32 v62, v62
	v_mul_f32_e32 v63, 0xbfb8aa3b, v65
	v_add_f32_e32 v54, 1.0, v54
	v_exp_f32_e32 v63, v63
	v_rcp_f32_e32 v54, v54
	v_add_f32_e32 v62, 1.0, v62
	v_rcp_f32_e32 v62, v62
	v_add_f32_e32 v63, 1.0, v63
	v_mul_f32_e32 v57, v114, v57
	v_mul_f32_e32 v54, v87, v54
	v_rcp_f32_e32 v63, v63
	v_mul_f32_e32 v57, 0x41000000, v57
	v_mul_f32_e32 v54, v115, v54
	v_mul_f32_e32 v54, 0x41000000, v54
	v_mul_f32_e32 v62, v64, v62
	v_min_f32_e64 v64, |v57|, s33
	v_bfi_b32 v64, s2, v64, v57
	v_min_f32_e64 v57, |v54|, s33
	v_mul_f32_e32 v62, v92, v62
	v_mul_f32_e32 v63, v65, v63
	v_bfi_b32 v54, s2, v57, v54
	v_mov_b32_e32 v57, v207
	v_mul_f32_e32 v62, 0x41000000, v62
	v_mul_f32_e32 v63, v93, v63
	v_cvt_pk_fp8_f32 v57, v64, v54
	v_mul_f32_e32 v63, 0x41000000, v63
	v_min_f32_e64 v65, |v62|, s33
	v_bfi_b32 v54, s2, v65, v62
	v_min_f32_e64 v62, |v63|, s33
	v_bfi_b32 v62, s2, v62, v63
	v_cvt_pk_fp8_f32 v57, v54, v62 op_sel:[0,0,1]
	v_lshlrev_b64 v[62:63], 11, v[130:131]
	v_mul_f32_e32 v54, 0x3b800000, v55
	v_lshl_add_u64 v[62:63], s[50:51], 0, v[62:63]
	v_pk_mul_f32 v[64:65], v[106:107], v[54:55] op_sel_hi:[1,0]
	v_lshl_add_u64 v[114:115], v[62:63], 0, v[206:207]
	v_pk_mul_f32 v[62:63], v[108:109], v[54:55] op_sel_hi:[1,0]
	v_pk_mul_f32 v[86:87], v[104:105], v[54:55] op_sel_hi:[1,0]
	v_pk_mul_f32 v[88:89], v[102:103], v[54:55] op_sel_hi:[1,0]
	v_pk_mul_f32 v[90:91], v[112:113], v[54:55] op_sel_hi:[1,0]
	v_pk_mul_f32 v[92:93], v[110:111], v[54:55] op_sel_hi:[1,0]
	v_mul_f32_e32 v55, 0xbfb8aa3b, v64
	v_exp_f32_e32 v55, v55
	v_mul_f32_e32 v102, 0xbfb8aa3b, v65
	v_exp_f32_e32 v102, v102
	global_store_dwordx2 v[114:115], v[56:57], off
	v_pk_mul_f32 v[100:101], v[100:101], v[54:55] op_sel_hi:[1,0]
	v_add_f32_e32 v55, 1.0, v55
	v_rcp_f32_e32 v103, v55
	v_pk_mul_f32 v[54:55], v[98:99], v[54:55] op_sel_hi:[1,0]
	v_add_f32_e32 v98, 1.0, v102
	v_rcp_f32_e32 v98, v98
	v_mul_f32_e32 v64, v64, v103
	v_mul_f32_e32 v64, v92, v64
	v_mul_f32_e32 v92, 0xbfb8aa3b, v62
	v_mul_f32_e32 v65, v65, v98
	v_exp_f32_e32 v92, v92
	v_mul_f32_e32 v65, v93, v65
	v_mul_f32_e32 v93, 0xbfb8aa3b, v63
	v_exp_f32_e32 v93, v93
	v_add_f32_e32 v92, 1.0, v92
	v_rcp_f32_e32 v92, v92
	v_mul_f32_e32 v64, 0x41000000, v64
	v_add_f32_e32 v93, 1.0, v93
	v_rcp_f32_e32 v93, v93
	v_mul_f32_e32 v62, v62, v92
	v_mul_f32_e32 v65, 0x41000000, v65
	v_mul_f32_e32 v62, v90, v62
	v_mul_f32_e32 v63, v63, v93
	v_min_f32_e64 v90, |v64|, s33
	v_mul_f32_e32 v62, 0x41000000, v62
	v_mul_f32_e32 v63, v91, v63
	v_bfi_b32 v64, s2, v90, v64
	v_min_f32_e64 v90, |v65|, s33
	v_mul_f32_e32 v63, 0x41000000, v63
	v_bfi_b32 v65, s2, v90, v65
	v_min_f32_e64 v90, |v62|, s33
	v_bfi_b32 v90, s2, v90, v62
	v_min_f32_e64 v62, |v63|, s33
	v_bfi_b32 v63, s2, v62, v63
	v_mov_b32_e32 v62, v207
	v_cvt_pk_fp8_f32 v62, v64, v65
	v_mul_f32_e32 v64, 0xbfb8aa3b, v89
	v_exp_f32_e32 v64, v64
	v_mul_f32_e32 v91, 0xbfb8aa3b, v88
	v_exp_f32_e32 v91, v91
	v_cvt_pk_fp8_f32 v62, v90, v63 op_sel:[0,0,1]
	v_add_f32_e32 v63, 1.0, v64
	v_rcp_f32_e32 v63, v63
	v_add_f32_e32 v65, 1.0, v91
	v_rcp_f32_e32 v65, v65
	v_or_b32_e32 v56, 16, v130
	v_mul_f32_e32 v63, v89, v63
	v_mul_f32_e32 v55, v55, v63
	v_mul_f32_e32 v63, 0xbfb8aa3b, v87
	v_exp_f32_e32 v63, v63
	v_mul_f32_e32 v64, v88, v65
	v_mul_f32_e32 v54, v54, v64
	v_mul_f32_e32 v64, 0xbfb8aa3b, v86
	v_exp_f32_e32 v64, v64
	v_add_f32_e32 v63, 1.0, v63
	v_rcp_f32_e32 v63, v63
	v_mul_f32_e32 v54, 0x41000000, v54
	v_add_f32_e32 v64, 1.0, v64
	v_rcp_f32_e32 v64, v64
	v_mul_f32_e32 v63, v87, v63
	v_mul_f32_e32 v63, v101, v63
	v_mul_f32_e32 v55, 0x41000000, v55
	v_mul_f32_e32 v65, 0x41000000, v63
	v_min_f32_e64 v63, |v54|, s33
	v_bfi_b32 v54, s2, v63, v54
	v_min_f32_e64 v63, |v55|, s33
	v_mul_f32_e32 v64, v86, v64
	v_bfi_b32 v55, s2, v63, v55
	v_mov_b32_e32 v63, v207
	v_mul_f32_e32 v64, v100, v64
	v_cvt_pk_fp8_f32 v63, v54, v55
	v_mul_f32_e32 v64, 0x41000000, v64
	v_ashrrev_i32_e32 v57, 31, v56
	v_min_f32_e64 v86, |v64|, s33
	v_min_f32_e64 v55, |v65|, s33
	v_lshlrev_b64 v[56:57], 11, v[56:57]
	v_bfi_b32 v54, s2, v86, v64
	v_bfi_b32 v55, s2, v55, v65
	v_cvt_pk_fp8_f32 v63, v54, v55 op_sel:[0,0,1]
	v_lshl_add_u64 v[54:55], s[50:51], 0, v[56:57]
	ds_read2_b32 v[56:57], v132 offset0:32 offset1:48
	v_lshl_add_u64 v[54:55], v[54:55], 0, v[206:207]
	global_store_dwordx2 v[54:55], v[62:63], off
	v_or_b32_e32 v54, 32, v130
	v_ashrrev_i32_e32 v55, 31, v54
	s_waitcnt lgkmcnt(0)
	v_mul_f32_e32 v56, 0x3b800000, v56
	v_pk_mul_f32 v[58:59], v[58:59], v[56:57] op_sel_hi:[1,0]
	v_pk_mul_f32 v[60:61], v[60:61], v[56:57] op_sel_hi:[1,0]
	v_mul_f32_e32 v86, 0xbfb8aa3b, v58
	v_mul_f32_e32 v87, 0xbfb8aa3b, v59
	v_exp_f32_e32 v86, v86
	v_exp_f32_e32 v87, v87
	v_pk_mul_f32 v[12:13], v[12:13], v[56:57] op_sel_hi:[1,0]
	v_pk_mul_f32 v[10:11], v[10:11], v[56:57] op_sel_hi:[1,0]
	v_pk_mul_f32 v[62:63], v[96:97], v[56:57] op_sel_hi:[1,0]
	v_pk_mul_f32 v[64:65], v[94:95], v[56:57] op_sel_hi:[1,0]
	v_pk_mul_f32 v[84:85], v[84:85], v[56:57] op_sel_hi:[1,0]
	v_add_f32_e32 v86, 1.0, v86
	v_pk_mul_f32 v[82:83], v[82:83], v[56:57] op_sel_hi:[1,0]
	v_add_f32_e32 v56, 1.0, v87
	v_rcp_f32_e32 v86, v86
	v_rcp_f32_e32 v56, v56
	v_mov_b64_e32 v[226:227], v[250:251]
	v_mov_b64_e32 v[250:251], v[232:233]
	v_mul_f32_e32 v58, v58, v86
	v_mul_f32_e32 v56, v59, v56
	v_mul_f32_e32 v59, 0xbfb8aa3b, v60
	v_mul_f32_e32 v58, v64, v58
	v_exp_f32_e32 v59, v59
	v_mul_f32_e32 v64, 0xbfb8aa3b, v61
	v_exp_f32_e32 v64, v64
	v_mul_f32_e32 v58, 0x41000000, v58
	v_add_f32_e32 v59, 1.0, v59
	v_rcp_f32_e32 v59, v59
	v_add_f32_e32 v64, 1.0, v64
	v_rcp_f32_e32 v64, v64
	v_mul_f32_e32 v56, v65, v56
	v_mul_f32_e32 v59, v60, v59
	v_mul_f32_e32 v56, 0x41000000, v56
	v_mul_f32_e32 v59, v62, v59
	v_mul_f32_e32 v60, v61, v64
	v_min_f32_e64 v61, |v58|, s33
	v_mul_f32_e32 v59, 0x41000000, v59
	v_mul_f32_e32 v60, v63, v60
	v_bfi_b32 v61, s2, v61, v58
	v_min_f32_e64 v58, |v56|, s33
	v_mul_f32_e32 v60, 0x41000000, v60
	v_bfi_b32 v56, s2, v58, v56
	v_min_f32_e64 v58, |v59|, s33
	v_bfi_b32 v59, s2, v58, v59
	v_min_f32_e64 v58, |v60|, s33
	v_bfi_b32 v60, s2, v58, v60
	v_mov_b32_e32 v58, v207
	v_cvt_pk_fp8_f32 v58, v61, v56
	v_mul_f32_e32 v56, 0xbfb8aa3b, v11
	v_exp_f32_e32 v56, v56
	v_mul_f32_e32 v62, 0xbfb8aa3b, v10
	v_exp_f32_e32 v62, v62
	v_cvt_pk_fp8_f32 v58, v59, v60 op_sel:[0,0,1]
	v_add_f32_e32 v56, 1.0, v56
	v_rcp_f32_e32 v56, v56
	v_add_f32_e32 v61, 1.0, v62
	v_mul_f32_e32 v59, 0xbfb8aa3b, v13
	v_rcp_f32_e32 v61, v61
	v_mul_f32_e32 v11, v11, v56
	v_mul_f32_e32 v56, 0xbfb8aa3b, v12
	v_exp_f32_e32 v56, v56
	v_exp_f32_e32 v59, v59
	v_mul_f32_e32 v10, v10, v61
	v_mul_f32_e32 v10, v82, v10
	v_add_f32_e32 v56, 1.0, v56
	v_rcp_f32_e32 v56, v56
	v_add_f32_e32 v59, 1.0, v59
	v_rcp_f32_e32 v59, v59
	v_mul_f32_e32 v10, 0x41000000, v10
	v_mul_f32_e32 v11, v83, v11
	v_mul_f32_e32 v11, 0x41000000, v11
	v_mul_f32_e32 v12, v12, v56
	v_min_f32_e64 v56, |v10|, s33
	v_bfi_b32 v10, s2, v56, v10
	v_min_f32_e64 v56, |v11|, s33
	v_mul_f32_e32 v13, v13, v59
	v_bfi_b32 v11, s2, v56, v11
	v_mov_b32_e32 v59, v207
	v_mul_f32_e32 v12, v84, v12
	v_mul_f32_e32 v13, v85, v13
	v_cvt_pk_fp8_f32 v59, v10, v11
	v_mul_f32_e32 v12, 0x41000000, v12
	v_mul_f32_e32 v13, 0x41000000, v13
	v_min_f32_e64 v56, |v12|, s33
	v_min_f32_e64 v11, |v13|, s33
	v_bfi_b32 v10, s2, v56, v12
	v_bfi_b32 v11, s2, v11, v13
	v_cvt_pk_fp8_f32 v59, v10, v11 op_sel:[0,0,1]
	v_lshlrev_b64 v[10:11], 11, v[54:55]
	v_lshl_add_u64 v[10:11], s[50:51], 0, v[10:11]
	v_mul_f32_e32 v12, 0x3b800000, v57
	v_lshl_add_u64 v[10:11], v[10:11], 0, v[206:207]
	v_pk_mul_f32 v[56:57], v[74:75], v[12:13] op_sel_hi:[1,0]
	global_store_dwordx2 v[10:11], v[58:59], off
	v_pk_mul_f32 v[54:55], v[76:77], v[12:13] op_sel_hi:[1,0]
	v_pk_mul_f32 v[58:59], v[72:73], v[12:13] op_sel_hi:[1,0]
	v_pk_mul_f32 v[60:61], v[70:71], v[12:13] op_sel_hi:[1,0]
	v_pk_mul_f32 v[62:63], v[80:81], v[12:13] op_sel_hi:[1,0]
	v_pk_mul_f32 v[64:65], v[78:79], v[12:13] op_sel_hi:[1,0]
	v_mul_f32_e32 v13, 0xbfb8aa3b, v56
	v_exp_f32_e32 v13, v13
	v_mul_f32_e32 v70, 0xbfb8aa3b, v57
	v_exp_f32_e32 v70, v70
	v_or_b32_e32 v10, 48, v130
	v_pk_mul_f32 v[68:69], v[68:69], v[12:13] op_sel_hi:[1,0]
	v_add_f32_e32 v13, 1.0, v13
	v_rcp_f32_e32 v71, v13
	v_pk_mul_f32 v[12:13], v[66:67], v[12:13] op_sel_hi:[1,0]
	v_add_f32_e32 v66, 1.0, v70
	v_rcp_f32_e32 v66, v66
	v_mul_f32_e32 v56, v56, v71
	v_mul_f32_e32 v56, v64, v56
	v_mul_f32_e32 v64, 0xbfb8aa3b, v54
	v_mul_f32_e32 v57, v57, v66
	v_exp_f32_e32 v64, v64
	v_mul_f32_e32 v57, v65, v57
	v_mul_f32_e32 v65, 0xbfb8aa3b, v55
	v_exp_f32_e32 v65, v65
	v_add_f32_e32 v64, 1.0, v64
	v_rcp_f32_e32 v64, v64
	v_mul_f32_e32 v56, 0x41000000, v56
	v_add_f32_e32 v65, 1.0, v65
	v_rcp_f32_e32 v65, v65
	v_mul_f32_e32 v54, v54, v64
	v_mul_f32_e32 v57, 0x41000000, v57
	v_mul_f32_e32 v54, v62, v54
	v_mul_f32_e32 v55, v55, v65
	v_min_f32_e64 v62, |v56|, s33
	v_mul_f32_e32 v54, 0x41000000, v54
	v_mul_f32_e32 v55, v63, v55
	v_bfi_b32 v56, s2, v62, v56
	v_min_f32_e64 v62, |v57|, s33
	v_mul_f32_e32 v55, 0x41000000, v55
	v_bfi_b32 v57, s2, v62, v57
	v_min_f32_e64 v62, |v54|, s33
	v_bfi_b32 v62, s2, v62, v54
	v_min_f32_e64 v54, |v55|, s33
	v_bfi_b32 v55, s2, v54, v55
	v_mov_b32_e32 v54, v207
	v_cvt_pk_fp8_f32 v54, v56, v57
	v_mul_f32_e32 v56, 0xbfb8aa3b, v61
	v_exp_f32_e32 v56, v56
	v_mul_f32_e32 v63, 0xbfb8aa3b, v60
	v_exp_f32_e32 v63, v63
	v_cvt_pk_fp8_f32 v54, v62, v55 op_sel:[0,0,1]
	v_add_f32_e32 v55, 1.0, v56
	v_rcp_f32_e32 v55, v55
	v_add_f32_e32 v57, 1.0, v63
	v_rcp_f32_e32 v57, v57
	v_ashrrev_i32_e32 v11, 31, v10
	v_mul_f32_e32 v55, v61, v55
	v_mul_f32_e32 v13, v13, v55
	v_mul_f32_e32 v55, 0xbfb8aa3b, v59
	v_exp_f32_e32 v55, v55
	v_mul_f32_e32 v56, v60, v57
	v_mul_f32_e32 v12, v12, v56
	v_mul_f32_e32 v56, 0xbfb8aa3b, v58
	v_exp_f32_e32 v56, v56
	v_add_f32_e32 v55, 1.0, v55
	v_rcp_f32_e32 v55, v55
	v_mul_f32_e32 v12, 0x41000000, v12
	v_add_f32_e32 v56, 1.0, v56
	v_rcp_f32_e32 v56, v56
	v_mul_f32_e32 v55, v59, v55
	v_mul_f32_e32 v55, v69, v55
	v_mul_f32_e32 v13, 0x41000000, v13
	v_mul_f32_e32 v57, 0x41000000, v55
	v_min_f32_e64 v55, |v12|, s33
	v_bfi_b32 v12, s2, v55, v12
	v_min_f32_e64 v55, |v13|, s33
	v_mul_f32_e32 v56, v58, v56
	v_bfi_b32 v13, s2, v55, v13
	v_mov_b32_e32 v55, v207
	v_mul_f32_e32 v56, v68, v56
	v_cvt_pk_fp8_f32 v55, v12, v13
	v_mul_f32_e32 v56, 0x41000000, v56
	v_min_f32_e64 v58, |v56|, s33
	v_min_f32_e64 v13, |v57|, s33
	v_bfi_b32 v12, s2, v58, v56
	v_bfi_b32 v13, s2, v13, v57
	v_cvt_pk_fp8_f32 v55, v12, v13 op_sel:[0,0,1]
	ds_read2_b32 v[12:13], v132 offset0:128 offset1:144
	v_lshlrev_b64 v[10:11], 11, v[10:11]
	v_lshl_add_u64 v[10:11], s[50:51], 0, v[10:11]
	v_lshl_add_u64 v[10:11], v[10:11], 0, v[206:207]
	global_store_dwordx2 v[10:11], v[54:55], off
	s_waitcnt lgkmcnt(0)
	v_mul_f32_e32 v10, 0x3b800000, v12
	v_pk_mul_f32 v[56:57], v[178:179], v[10:11] op_sel_hi:[1,0]
	v_pk_mul_f32 v[54:55], v[180:181], v[10:11] op_sel_hi:[1,0]
	v_pk_mul_f32 v[58:59], v[176:177], v[10:11] op_sel_hi:[1,0]
	v_pk_mul_f32 v[60:61], v[174:175], v[10:11] op_sel_hi:[1,0]
	v_pk_mul_f32 v[62:63], v[184:185], v[10:11] op_sel_hi:[1,0]
	v_pk_mul_f32 v[64:65], v[182:183], v[10:11] op_sel_hi:[1,0]
	v_mul_f32_e32 v11, 0xbfb8aa3b, v56
	v_exp_f32_e32 v11, v11
	v_mul_f32_e32 v12, 0xbfb8aa3b, v57
	v_exp_f32_e32 v12, v12
	v_pk_mul_f32 v[52:53], v[52:53], v[10:11] op_sel_hi:[1,0]
	v_add_f32_e32 v11, 1.0, v11
	v_rcp_f32_e32 v66, v11
	v_pk_mul_f32 v[10:11], v[50:51], v[10:11] op_sel_hi:[1,0]
	v_mul_f32_e32 v51, 0xbfb8aa3b, v54
	v_exp_f32_e32 v51, v51
	v_mul_f32_e32 v50, v56, v66
	v_mul_f32_e32 v56, 0xbfb8aa3b, v55
	v_exp_f32_e32 v56, v56
	v_add_f32_e32 v12, 1.0, v12
	v_rcp_f32_e32 v12, v12
	v_add_f32_e32 v51, 1.0, v51
	v_rcp_f32_e32 v51, v51
	v_add_f32_e32 v56, 1.0, v56
	v_rcp_f32_e32 v56, v56
	v_mul_f32_e32 v50, v64, v50
	v_mul_f32_e32 v12, v57, v12
	v_mul_f32_e32 v50, 0x41000000, v50
	v_mul_f32_e32 v12, v65, v12
	v_mul_f32_e32 v51, v54, v51
	v_mul_f32_e32 v12, 0x41000000, v12
	v_mul_f32_e32 v51, v62, v51
	v_mul_f32_e32 v54, v55, v56
	v_min_f32_e64 v55, |v50|, s33
	v_mul_f32_e32 v51, 0x41000000, v51
	v_mul_f32_e32 v54, v63, v54
	v_bfi_b32 v55, s2, v55, v50
	v_min_f32_e64 v50, |v12|, s33
	v_mul_f32_e32 v56, 0xbfb8aa3b, v60
	v_mul_f32_e32 v54, 0x41000000, v54
	v_bfi_b32 v12, s2, v50, v12
	v_min_f32_e64 v50, |v51|, s33
	v_exp_f32_e32 v56, v56
	v_bfi_b32 v51, s2, v50, v51
	v_min_f32_e64 v50, |v54|, s33
	v_bfi_b32 v54, s2, v50, v54
	v_mov_b32_e32 v50, v207
	v_cvt_pk_fp8_f32 v50, v55, v12
	v_mul_f32_e32 v12, 0xbfb8aa3b, v61
	v_exp_f32_e32 v12, v12
	v_add_f32_e32 v55, 1.0, v56
	v_rcp_f32_e32 v55, v55
	v_cvt_pk_fp8_f32 v50, v51, v54 op_sel:[0,0,1]
	v_add_f32_e32 v12, 1.0, v12
	v_rcp_f32_e32 v12, v12
	v_mul_f32_e32 v51, v60, v55
	v_mul_f32_e32 v10, v10, v51
	v_mul_f32_e32 v51, 0xbfb8aa3b, v58
	v_exp_f32_e32 v51, v51
	v_mul_f32_e32 v12, v61, v12
	v_mul_f32_e32 v11, v11, v12
	v_mul_f32_e32 v12, 0xbfb8aa3b, v59
	v_exp_f32_e32 v12, v12
	v_add_f32_e32 v51, 1.0, v51
	v_rcp_f32_e32 v51, v51
	v_mul_f32_e32 v10, 0x41000000, v10
	v_add_f32_e32 v12, 1.0, v12
	v_rcp_f32_e32 v12, v12
	v_mul_f32_e32 v51, v58, v51
	v_mul_f32_e32 v51, v52, v51
	v_mul_f32_e32 v11, 0x41000000, v11
	v_mul_f32_e32 v52, 0x41000000, v51
	v_min_f32_e64 v51, |v10|, s33
	v_bfi_b32 v10, s2, v51, v10
	v_min_f32_e64 v51, |v11|, s33
	v_mul_f32_e32 v12, v59, v12
	v_bfi_b32 v11, s2, v51, v11
	v_mov_b32_e32 v51, v207
	v_mul_f32_e32 v12, v53, v12
	v_cvt_pk_fp8_f32 v51, v10, v11
	v_mul_f32_e32 v12, 0x41000000, v12
	v_min_f32_e64 v53, |v52|, s33
	v_min_f32_e64 v11, |v12|, s33
	v_bfi_b32 v10, s2, v53, v52
	v_bfi_b32 v11, s2, v11, v12
	v_cvt_pk_fp8_f32 v51, v10, v11 op_sel:[0,0,1]
	v_add_co_u32_e32 v10, vcc, s0, v114
	s_mov_b32 s0, 0x48000
	s_nop 0
	v_addc_co_u32_e32 v11, vcc, 0, v115, vcc
	global_store_dwordx2 v[10:11], v[50:51], off
	v_mul_f32_e32 v10, 0x3b800000, v13
	v_pk_mul_f32 v[42:43], v[42:43], v[10:11] op_sel_hi:[1,0]
	v_pk_mul_f32 v[12:13], v[44:45], v[10:11] op_sel_hi:[1,0]
	v_pk_mul_f32 v[40:41], v[40:41], v[10:11] op_sel_hi:[1,0]
	v_pk_mul_f32 v[38:39], v[38:39], v[10:11] op_sel_hi:[1,0]
	v_pk_mul_f32 v[44:45], v[48:49], v[10:11] op_sel_hi:[1,0]
	v_pk_mul_f32 v[46:47], v[46:47], v[10:11] op_sel_hi:[1,0]
	v_mul_f32_e32 v11, 0xbfb8aa3b, v42
	v_exp_f32_e32 v11, v11
	v_mul_f32_e32 v48, 0xbfb8aa3b, v43
	v_exp_f32_e32 v48, v48
	v_pk_mul_f32 v[36:37], v[36:37], v[10:11] op_sel_hi:[1,0]
	v_add_f32_e32 v11, 1.0, v11
	v_rcp_f32_e32 v49, v11
	v_pk_mul_f32 v[10:11], v[34:35], v[10:11] op_sel_hi:[1,0]
	v_add_f32_e32 v34, 1.0, v48
	v_rcp_f32_e32 v34, v34
	v_mul_f32_e32 v35, v42, v49
	v_mul_f32_e32 v42, 0xbfb8aa3b, v12
	v_exp_f32_e32 v42, v42
	v_mul_f32_e32 v34, v43, v34
	v_mul_f32_e32 v43, 0xbfb8aa3b, v13
	v_exp_f32_e32 v43, v43
	v_add_f32_e32 v42, 1.0, v42
	v_rcp_f32_e32 v42, v42
	v_mul_f32_e32 v35, v46, v35
	v_add_f32_e32 v43, 1.0, v43
	v_rcp_f32_e32 v43, v43
	v_mul_f32_e32 v35, 0x41000000, v35
	v_mul_f32_e32 v34, v47, v34
	v_mul_f32_e32 v12, v12, v42
	v_mul_f32_e32 v34, 0x41000000, v34
	v_mul_f32_e32 v12, v44, v12
	v_mul_f32_e32 v13, v13, v43
	v_min_f32_e64 v42, |v35|, s33
	v_mul_f32_e32 v12, 0x41000000, v12
	v_mul_f32_e32 v13, v45, v13
	v_bfi_b32 v35, s2, v42, v35
	v_min_f32_e64 v42, |v34|, s33
	v_mul_f32_e32 v13, 0x41000000, v13
	v_bfi_b32 v34, s2, v42, v34
	v_min_f32_e64 v42, |v12|, s33
	v_bfi_b32 v42, s2, v42, v12
	v_min_f32_e64 v12, |v13|, s33
	v_bfi_b32 v13, s2, v12, v13
	v_mov_b32_e32 v12, v207
	v_cvt_pk_fp8_f32 v12, v35, v34
	v_mul_f32_e32 v34, 0xbfb8aa3b, v39
	v_exp_f32_e32 v34, v34
	v_mul_f32_e32 v43, 0xbfb8aa3b, v38
	v_exp_f32_e32 v43, v43
	v_cvt_pk_fp8_f32 v12, v42, v13 op_sel:[0,0,1]
	v_add_f32_e32 v13, 1.0, v34
	v_rcp_f32_e32 v13, v13
	v_add_f32_e32 v35, 1.0, v43
	v_rcp_f32_e32 v35, v35
	v_mul_f32_e32 v13, v39, v13
	v_mul_f32_e32 v11, v11, v13
	v_mul_f32_e32 v13, 0xbfb8aa3b, v41
	v_exp_f32_e32 v13, v13
	v_mul_f32_e32 v34, v38, v35
	v_mul_f32_e32 v10, v10, v34
	v_mul_f32_e32 v34, 0xbfb8aa3b, v40
	v_exp_f32_e32 v34, v34
	v_add_f32_e32 v13, 1.0, v13
	v_rcp_f32_e32 v13, v13
	v_mul_f32_e32 v10, 0x41000000, v10
	v_add_f32_e32 v34, 1.0, v34
	v_rcp_f32_e32 v34, v34
	v_mul_f32_e32 v13, v41, v13
	v_mul_f32_e32 v13, v37, v13
	v_mul_f32_e32 v11, 0x41000000, v11
	v_mul_f32_e32 v35, 0x41000000, v13
	v_min_f32_e64 v13, |v10|, s33
	v_bfi_b32 v10, s2, v13, v10
	v_min_f32_e64 v13, |v11|, s33
	v_mul_f32_e32 v34, v40, v34
	v_bfi_b32 v11, s2, v13, v11
	v_mov_b32_e32 v13, v207
	v_mul_f32_e32 v34, v36, v34
	v_cvt_pk_fp8_f32 v13, v10, v11
	v_mul_f32_e32 v34, 0x41000000, v34
	v_min_f32_e64 v36, |v34|, s33
	v_min_f32_e64 v11, |v35|, s33
	v_bfi_b32 v10, s2, v36, v34
	v_bfi_b32 v11, s2, v11, v35
	v_cvt_pk_fp8_f32 v13, v10, v11 op_sel:[0,0,1]
	ds_read2_b32 v[10:11], v132 offset0:160 offset1:176
	v_add_co_u32_e32 v34, vcc, s0, v114
	s_mov_b32 s0, 0x50000
	s_nop 0
	v_addc_co_u32_e32 v35, vcc, 0, v115, vcc
	s_waitcnt lgkmcnt(0)
	v_mul_f32_e32 v10, 0x3b800000, v10
	v_pk_mul_f32 v[26:27], v[26:27], v[10:11] op_sel_hi:[1,0]
	global_store_dwordx2 v[34:35], v[12:13], off
	v_pk_mul_f32 v[12:13], v[28:29], v[10:11] op_sel_hi:[1,0]
	v_pk_mul_f32 v[28:29], v[32:33], v[10:11] op_sel_hi:[1,0]
	v_mul_f32_e32 v32, 0xbfb8aa3b, v26
	v_mul_f32_e32 v33, 0xbfb8aa3b, v27
	v_exp_f32_e32 v32, v32
	v_exp_f32_e32 v33, v33
	v_pk_mul_f32 v[24:25], v[24:25], v[10:11] op_sel_hi:[1,0]
	v_pk_mul_f32 v[22:23], v[22:23], v[10:11] op_sel_hi:[1,0]
	v_pk_mul_f32 v[30:31], v[30:31], v[10:11] op_sel_hi:[1,0]
	v_pk_mul_f32 v[20:21], v[20:21], v[10:11] op_sel_hi:[1,0]
	v_add_f32_e32 v32, 1.0, v32
	v_pk_mul_f32 v[18:19], v[18:19], v[10:11] op_sel_hi:[1,0]
	v_add_f32_e32 v10, 1.0, v33
	v_rcp_f32_e32 v32, v32
	v_rcp_f32_e32 v10, v10
	v_mul_f32_e32 v26, v26, v32
	v_mul_f32_e32 v10, v27, v10
	v_mul_f32_e32 v27, 0xbfb8aa3b, v12
	v_mul_f32_e32 v26, v30, v26
	v_exp_f32_e32 v27, v27
	v_mul_f32_e32 v30, 0xbfb8aa3b, v13
	v_exp_f32_e32 v30, v30
	v_mul_f32_e32 v26, 0x41000000, v26
	v_add_f32_e32 v27, 1.0, v27
	v_rcp_f32_e32 v27, v27
	v_add_f32_e32 v30, 1.0, v30
	v_rcp_f32_e32 v30, v30
	v_mul_f32_e32 v10, v31, v10
	v_mul_f32_e32 v12, v12, v27
	v_mul_f32_e32 v10, 0x41000000, v10
	v_mul_f32_e32 v12, v28, v12
	v_mul_f32_e32 v13, v13, v30
	v_min_f32_e64 v27, |v26|, s33
	v_mul_f32_e32 v12, 0x41000000, v12
	v_mul_f32_e32 v13, v29, v13
	v_bfi_b32 v26, s2, v27, v26
	v_min_f32_e64 v27, |v10|, s33
	v_mul_f32_e32 v13, 0x41000000, v13
	v_bfi_b32 v10, s2, v27, v10
	v_min_f32_e64 v27, |v12|, s33
	v_mul_f32_e32 v28, 0xbfb8aa3b, v22
	v_bfi_b32 v27, s2, v27, v12
	v_min_f32_e64 v12, |v13|, s33
	v_exp_f32_e32 v28, v28
	v_bfi_b32 v13, s2, v12, v13
	v_mov_b32_e32 v12, v207
	v_cvt_pk_fp8_f32 v12, v26, v10
	v_mul_f32_e32 v10, 0xbfb8aa3b, v23
	v_exp_f32_e32 v10, v10
	v_add_f32_e32 v26, 1.0, v28
	v_rcp_f32_e32 v26, v26
	v_cvt_pk_fp8_f32 v12, v27, v13 op_sel:[0,0,1]
	v_add_f32_e32 v10, 1.0, v10
	v_rcp_f32_e32 v10, v10
	v_mul_f32_e32 v13, v22, v26
	v_mul_f32_e32 v13, v18, v13
	v_mul_f32_e32 v18, 0xbfb8aa3b, v24
	v_exp_f32_e32 v18, v18
	v_mul_f32_e32 v10, v23, v10
	v_mul_f32_e32 v10, v19, v10
	v_mul_f32_e32 v19, 0xbfb8aa3b, v25
	v_exp_f32_e32 v19, v19
	v_add_f32_e32 v18, 1.0, v18
	v_rcp_f32_e32 v18, v18
	v_mul_f32_e32 v13, 0x41000000, v13
	v_add_f32_e32 v19, 1.0, v19
	v_rcp_f32_e32 v19, v19
	v_mul_f32_e32 v18, v24, v18
	v_mul_f32_e32 v10, 0x41000000, v10
	v_mul_f32_e32 v18, v20, v18
	v_min_f32_e64 v20, |v13|, s33
	v_bfi_b32 v20, s2, v20, v13
	v_min_f32_e64 v13, |v10|, s33
	v_mul_f32_e32 v19, v25, v19
	v_bfi_b32 v10, s2, v13, v10
	v_mov_b32_e32 v13, v207
	v_mul_f32_e32 v18, 0x41000000, v18
	v_mul_f32_e32 v19, v21, v19
	v_cvt_pk_fp8_f32 v13, v20, v10
	v_mul_f32_e32 v19, 0x41000000, v19
	v_min_f32_e64 v21, |v18|, s33
	v_bfi_b32 v10, s2, v21, v18
	v_min_f32_e64 v18, |v19|, s33
	v_bfi_b32 v18, s2, v18, v19
	v_cvt_pk_fp8_f32 v13, v10, v18 op_sel:[0,0,1]
	v_add_co_u32_e32 v18, vcc, s0, v114
	v_mul_f32_e32 v10, 0x3b800000, v11
	s_nop 0
	v_addc_co_u32_e32 v19, vcc, 0, v115, vcc
	global_store_dwordx2 v[18:19], v[12:13], off
	v_pk_mul_f32 v[18:19], v[170:171], v[10:11] op_sel_hi:[1,0]
	v_pk_mul_f32 v[12:13], v[172:173], v[10:11] op_sel_hi:[1,0]
	v_pk_mul_f32 v[8:9], v[8:9], v[10:11] op_sel_hi:[1,0]
	v_pk_mul_f32 v[6:7], v[6:7], v[10:11] op_sel_hi:[1,0]
	v_pk_mul_f32 v[16:17], v[16:17], v[10:11] op_sel_hi:[1,0]
	v_pk_mul_f32 v[14:15], v[14:15], v[10:11] op_sel_hi:[1,0]
	v_mul_f32_e32 v11, 0xbfb8aa3b, v18
	v_exp_f32_e32 v11, v11
	v_mul_f32_e32 v20, 0xbfb8aa3b, v19
	v_exp_f32_e32 v20, v20
	s_mov_b64 s[0:1], -1
	v_pk_mul_f32 v[4:5], v[4:5], v[10:11] op_sel_hi:[1,0]
	v_add_f32_e32 v11, 1.0, v11
	v_rcp_f32_e32 v11, v11
	s_nop 0
	v_pk_mul_f32 v[2:3], v[2:3], v[10:11] op_sel_hi:[1,0]
	v_add_f32_e32 v10, 1.0, v20
	v_rcp_f32_e32 v10, v10
	v_mul_f32_e32 v11, v18, v11
	v_mul_f32_e32 v11, v14, v11
	v_mul_f32_e32 v14, 0xbfb8aa3b, v12
	v_mul_f32_e32 v10, v19, v10
	v_exp_f32_e32 v14, v14
	v_mul_f32_e32 v10, v15, v10
	v_mul_f32_e32 v15, 0xbfb8aa3b, v13
	v_exp_f32_e32 v15, v15
	v_add_f32_e32 v14, 1.0, v14
	v_rcp_f32_e32 v14, v14
	v_mul_f32_e32 v11, 0x41000000, v11
	v_add_f32_e32 v15, 1.0, v15
	v_rcp_f32_e32 v15, v15
	v_mul_f32_e32 v12, v12, v14
	v_mul_f32_e32 v10, 0x41000000, v10
	v_mul_f32_e32 v12, v16, v12
	v_mul_f32_e32 v13, v13, v15
	v_min_f32_e64 v14, |v11|, s33
	v_mul_f32_e32 v12, 0x41000000, v12
	v_mul_f32_e32 v13, v17, v13
	v_bfi_b32 v11, s2, v14, v11
	v_min_f32_e64 v14, |v10|, s33
	v_mul_f32_e32 v13, 0x41000000, v13
	v_bfi_b32 v14, s2, v14, v10
	v_min_f32_e64 v10, |v12|, s33
	v_bfi_b32 v12, s2, v10, v12
	v_min_f32_e64 v10, |v13|, s33
	v_bfi_b32 v13, s2, v10, v13
	v_mov_b32_e32 v10, v207
	v_mul_f32_e32 v15, 0xbfb8aa3b, v6
	v_exp_f32_e32 v15, v15
	v_cvt_pk_fp8_f32 v10, v11, v14
	v_mul_f32_e32 v11, 0xbfb8aa3b, v7
	v_exp_f32_e32 v11, v11
	v_add_f32_e32 v14, 1.0, v15
	v_rcp_f32_e32 v14, v14
	v_cvt_pk_fp8_f32 v10, v12, v13 op_sel:[0,0,1]
	v_add_f32_e32 v11, 1.0, v11
	v_rcp_f32_e32 v11, v11
	v_mul_f32_e32 v6, v6, v14
	v_mul_f32_e32 v2, v2, v6
	v_mul_f32_e32 v2, 0x41000000, v2
	v_mul_f32_e32 v6, v7, v11
	v_mul_f32_e32 v3, v3, v6
	v_mul_f32_e32 v6, 0xbfb8aa3b, v9
	v_exp_f32_e32 v6, v6
	v_mul_f32_e32 v7, 0xbfb8aa3b, v8
	v_exp_f32_e32 v7, v7
	v_mul_f32_e32 v3, 0x41000000, v3
	v_add_f32_e32 v6, 1.0, v6
	v_rcp_f32_e32 v6, v6
	v_add_f32_e32 v7, 1.0, v7
	v_rcp_f32_e32 v7, v7
	v_mov_b32_e32 v11, v207
	v_mul_f32_e32 v6, v9, v6
	v_mul_f32_e32 v5, v5, v6
	v_min_f32_e64 v6, |v2|, s33
	v_bfi_b32 v2, s2, v6, v2
	v_min_f32_e64 v6, |v3|, s33
	v_mul_f32_e32 v7, v8, v7
	v_bfi_b32 v3, s2, v6, v3
	v_mul_f32_e32 v4, v4, v7
	v_cvt_pk_fp8_f32 v11, v2, v3
	v_mul_f32_e32 v4, 0x41000000, v4
	v_mul_f32_e32 v5, 0x41000000, v5
	v_min_f32_e64 v6, |v4|, s33
	v_min_f32_e64 v3, |v5|, s33
	v_bfi_b32 v2, s2, v6, v4
	v_bfi_b32 v3, s2, v3, v5
	v_cvt_pk_fp8_f32 v11, v2, v3 op_sel:[0,0,1]
	v_add_co_u32_e32 v2, vcc, 0x58000, v114
	s_nop 1
	v_addc_co_u32_e32 v3, vcc, 0, v115, vcc
	s_and_b64 vcc, exec, s[38:39]
	global_store_dwordx2 v[2:3], v[10:11], off
	s_cmp_lt_i32 s100, 0
	s_cbranch_scc1 .Lfz_e_skip
	v_readlane_b32 s4, v253, 0
	v_readlane_b32 s5, v253, 1
	s_lshr_b32 s73, s100, 9
	s_mul_i32 s74, s73, 0xaaab
	s_lshr_b32 s74, s74, 17
	s_mul_i32 s75, s74, 3
	s_sub_i32 s73, s73, s75
	s_load_dwordx2 s[4:5], s[4:5], 0xa0
	v_readlane_b32 s23, v255, 55
	s_and_b32 s101, s100, 0x1ff
	s_add_i32 s23, s23, 1
	s_lshl_b32 s75, s23, 27
	s_lshl_b32 s100, s74, 22
	s_add_i32 s75, s75, s100
	s_and_b32 s100, s101, 31
	s_lshl_b32 s100, s100, 17
	s_add_i32 s75, s75, s100
	s_lshl_b32 s100, s73, 15
	s_add_i32 s75, s75, s100
	s_lshr_b32 s100, s101, 5
	s_lshl_b32 s100, s100, 6
	s_add_i32 s75, s75, s100
	s_add_u32 s75, s75, 0x3900000
	s_lshl_b32 s23, s23, 26
	s_lshl_b32 s74, s74, 21
	s_add_i32 s23, s23, s74
	s_and_b32 s74, s101, 15
	s_lshl_b32 s74, s74, 17
	s_add_i32 s23, s23, s74
	s_lshr_b32 s74, s101, 4
	s_lshl_b32 s74, s74, 6
	s_add_i32 s23, s23, s74
	s_add_u32 s23, s23, 0x23900000
	s_cmp_lt_u32 s73, 2
	s_cselect_b32 s75, s75, s23
	s_cselect_b32 s74, 12, 13
	s_mov_b32 s101, 0x800
	s_cselect_b32 s101, 0x400, s101
	s_mov_b32 s23, 0
	s_cselect_b32 s23, 0x8000, s23
	v_and_b32_e32 v224, 15, v0
	v_bfe_u32 v225, v0, 4, 2
	v_lshlrev_b32_e32 v202, s74, v224
	v_lshrrev_b32_e32 v224, 3, v224
	v_mul_u32_u24_e32 v224, s23, v224
	v_lshlrev_b32_e32 v225, 4, v225
	v_add3_u32 v202, v202, v224, v225
	v_mov_b32_e32 v204, 0x42800000
	v_mov_b32_e32 v205, 0x42800000
	v_mov_b32_e32 v203, 0xc3e00000
	s_waitcnt lgkmcnt(0)
	s_add_u32 s4, s4, s75
	s_addc_u32 s5, s5, 0
	s_waitcnt vmcnt(8)
	v_pk_mul_f32 v[134:135], v[134:135], v[204:205]
	v_pk_mul_f32 v[136:137], v[136:137], v[204:205]
	v_pk_mul_f32 v[138:139], v[138:139], v[204:205]
	v_pk_mul_f32 v[140:141], v[140:141], v[204:205]
	v_pk_mul_f32 v[142:143], v[142:143], v[204:205]
	v_pk_mul_f32 v[144:145], v[144:145], v[204:205]
	v_pk_mul_f32 v[146:147], v[146:147], v[204:205]
	v_pk_mul_f32 v[148:149], v[148:149], v[204:205]
	v_pk_mul_f32 v[150:151], v[150:151], v[204:205]
	v_pk_mul_f32 v[152:153], v[152:153], v[204:205]
	v_pk_mul_f32 v[154:155], v[154:155], v[204:205]
	v_pk_mul_f32 v[156:157], v[156:157], v[204:205]
	v_pk_mul_f32 v[158:159], v[158:159], v[204:205]
	v_pk_mul_f32 v[160:161], v[160:161], v[204:205]
	v_pk_mul_f32 v[162:163], v[162:163], v[204:205]
	v_pk_mul_f32 v[164:165], v[164:165], v[204:205]
	v_pk_mul_f32 v[166:167], v[166:167], v[204:205]
	v_pk_mul_f32 v[168:169], v[168:169], v[204:205]
	v_pk_mul_f32 v[186:187], v[186:187], v[204:205]
	v_pk_mul_f32 v[188:189], v[188:189], v[204:205]
	v_pk_mul_f32 v[190:191], v[190:191], v[204:205]
	v_pk_mul_f32 v[192:193], v[192:193], v[204:205]
	v_pk_mul_f32 v[208:209], v[208:209], v[204:205]
	v_pk_mul_f32 v[210:211], v[210:211], v[204:205]
	v_pk_mul_f32 v[212:213], v[212:213], v[204:205]
	v_pk_mul_f32 v[214:215], v[214:215], v[204:205]
	v_pk_mul_f32 v[216:217], v[216:217], v[204:205]
	v_pk_mul_f32 v[218:219], v[218:219], v[204:205]
	v_pk_mul_f32 v[220:221], v[220:221], v[204:205]
	v_pk_mul_f32 v[222:223], v[222:223], v[204:205]
	v_pk_mul_f32 v[234:235], v[234:235], v[204:205]
	v_pk_mul_f32 v[236:237], v[236:237], v[204:205]
	v_med3_f32 v134, v134, v203, s33
	v_med3_f32 v135, v135, v203, s33
	v_med3_f32 v136, v136, v203, s33
	v_med3_f32 v137, v137, v203, s33
	v_med3_f32 v138, v138, v203, s33
	v_med3_f32 v139, v139, v203, s33
	v_med3_f32 v140, v140, v203, s33
	v_med3_f32 v141, v141, v203, s33
	v_med3_f32 v142, v142, v203, s33
	v_med3_f32 v143, v143, v203, s33
	v_med3_f32 v144, v144, v203, s33
	v_med3_f32 v145, v145, v203, s33
	v_med3_f32 v146, v146, v203, s33
	v_med3_f32 v147, v147, v203, s33
	v_med3_f32 v148, v148, v203, s33
	v_med3_f32 v149, v149, v203, s33
	v_med3_f32 v150, v150, v203, s33
	v_med3_f32 v151, v151, v203, s33
	v_med3_f32 v152, v152, v203, s33
	v_med3_f32 v153, v153, v203, s33
	v_med3_f32 v154, v154, v203, s33
	v_med3_f32 v155, v155, v203, s33
	v_med3_f32 v156, v156, v203, s33
	v_med3_f32 v157, v157, v203, s33
	v_med3_f32 v158, v158, v203, s33
	v_med3_f32 v159, v159, v203, s33
	v_med3_f32 v160, v160, v203, s33
	v_med3_f32 v161, v161, v203, s33
	v_med3_f32 v162, v162, v203, s33
	v_med3_f32 v163, v163, v203, s33
	v_med3_f32 v164, v164, v203, s33
	v_med3_f32 v165, v165, v203, s33
	v_med3_f32 v166, v166, v203, s33
	v_med3_f32 v167, v167, v203, s33
	v_med3_f32 v168, v168, v203, s33
	v_med3_f32 v169, v169, v203, s33
	v_med3_f32 v186, v186, v203, s33
	v_med3_f32 v187, v187, v203, s33
	v_med3_f32 v188, v188, v203, s33
	v_med3_f32 v189, v189, v203, s33
	v_med3_f32 v190, v190, v203, s33
	v_med3_f32 v191, v191, v203, s33
	v_med3_f32 v192, v192, v203, s33
	v_med3_f32 v193, v193, v203, s33
	v_med3_f32 v208, v208, v203, s33
	v_med3_f32 v209, v209, v203, s33
	v_med3_f32 v210, v210, v203, s33
	v_med3_f32 v211, v211, v203, s33
	v_med3_f32 v212, v212, v203, s33
	v_med3_f32 v213, v213, v203, s33
	v_med3_f32 v214, v214, v203, s33
	v_med3_f32 v215, v215, v203, s33
	v_med3_f32 v216, v216, v203, s33
	v_med3_f32 v217, v217, v203, s33
	v_med3_f32 v218, v218, v203, s33
	v_med3_f32 v219, v219, v203, s33
	v_med3_f32 v220, v220, v203, s33
	v_med3_f32 v221, v221, v203, s33
	v_med3_f32 v222, v222, v203, s33
	v_med3_f32 v223, v223, v203, s33
	v_med3_f32 v234, v234, v203, s33
	v_med3_f32 v235, v235, v203, s33
	v_med3_f32 v236, v236, v203, s33
	v_med3_f32 v237, v237, v203, s33
	v_cvt_pk_fp8_f32 v242, v134, v138
	v_cvt_pk_fp8_f32 v243, v150, v154
	v_cvt_pk_fp8_f32 v244, v166, v186
	v_cvt_pk_fp8_f32 v245, v212, v216
	v_cvt_pk_fp8_f32 v242, v142, v146 op_sel:[0,0,1]
	v_cvt_pk_fp8_f32 v243, v158, v162 op_sel:[0,0,1]
	v_cvt_pk_fp8_f32 v244, v190, v208 op_sel:[0,0,1]
	v_cvt_pk_fp8_f32 v245, v220, v234 op_sel:[0,0,1]
	s_nop 1
	global_store_dwordx4 v202, v[242:245], s[4:5]
	s_add_u32 s4, s4, s101
	s_addc_u32 s5, s5, 0
	v_cvt_pk_fp8_f32 v246, v135, v139
	v_cvt_pk_fp8_f32 v247, v151, v155
	v_cvt_pk_fp8_f32 v248, v167, v187
	v_cvt_pk_fp8_f32 v249, v213, v217
	v_cvt_pk_fp8_f32 v246, v143, v147 op_sel:[0,0,1]
	v_cvt_pk_fp8_f32 v247, v159, v163 op_sel:[0,0,1]
	v_cvt_pk_fp8_f32 v248, v191, v209 op_sel:[0,0,1]
	v_cvt_pk_fp8_f32 v249, v221, v235 op_sel:[0,0,1]
	s_nop 1
	global_store_dwordx4 v202, v[246:249], s[4:5]
	s_add_u32 s4, s4, s101
	s_addc_u32 s5, s5, 0
	v_cvt_pk_fp8_f32 v242, v136, v140
	v_cvt_pk_fp8_f32 v243, v152, v156
	v_cvt_pk_fp8_f32 v244, v168, v188
	v_cvt_pk_fp8_f32 v245, v214, v218
	v_cvt_pk_fp8_f32 v242, v144, v148 op_sel:[0,0,1]
	v_cvt_pk_fp8_f32 v243, v160, v164 op_sel:[0,0,1]
	v_cvt_pk_fp8_f32 v244, v192, v210 op_sel:[0,0,1]
	v_cvt_pk_fp8_f32 v245, v222, v236 op_sel:[0,0,1]
	s_nop 1
	global_store_dwordx4 v202, v[242:245], s[4:5]
	s_add_u32 s4, s4, s101
	s_addc_u32 s5, s5, 0
	v_cvt_pk_fp8_f32 v246, v137, v141
	v_cvt_pk_fp8_f32 v247, v153, v157
	v_cvt_pk_fp8_f32 v248, v169, v189
	v_cvt_pk_fp8_f32 v249, v215, v219
	v_cvt_pk_fp8_f32 v246, v145, v149 op_sel:[0,0,1]
	v_cvt_pk_fp8_f32 v247, v161, v165 op_sel:[0,0,1]
	v_cvt_pk_fp8_f32 v248, v193, v211 op_sel:[0,0,1]
	v_cvt_pk_fp8_f32 v249, v223, v237 op_sel:[0,0,1]
	s_nop 1
	global_store_dwordx4 v202, v[246:249], s[4:5]
